# baseline (speedup 1.0000x reference)
.LBB0_71:
	s_andn2_b64 vcc, exec, s[4:5]
	s_cbranch_vccnz .LBB0_114
	s_and_b32 s4, s2, 7
	s_ashr_i32 s2, s2, 3
	s_mul_hi_i32 s3, s2, 0x2aaaaaab
	s_load_dwordx2 s[0:1], s[0:1], 0x0
	s_lshr_b32 s5, s3, 31
	s_ashr_i32 s3, s3, 2
	s_add_i32 s5, s3, s5
	s_mul_i32 s7, s5, 0x9a
	s_mul_i32 s3, s5, 24
	s_min_i32 s6, s7, 0x99
	s_sub_i32 s2, s2, s3
	s_addk_i32 s6, 0x9a
	s_mul_i32 s3, s4, 0xe6400
	s_waitcnt lgkmcnt(0)
	s_add_u32 s10, s0, s3
	s_addc_u32 s11, s1, 0
	s_lshl_b32 s0, s2, 5
	s_ashr_i32 s1, s0, 31
	v_and_b32_e32 v2, 31, v0
	s_lshl_b64 s[2:3], s[0:1], 2
	v_lshrrev_b32_e32 v1, 5, v0
	s_add_u32 s2, s10, s2
	v_lshlrev_b32_e32 v4, 2, v2
	v_mov_b32_e32 v2, 0
	s_addc_u32 s3, s11, s3
	v_mov_b32_e32 v5, v2
	v_add_u32_e32 v1, s7, v1
	v_lshl_add_u64 v[6:7], s[2:3], 0, v[4:5]
	v_mul_u32_u24_e32 v25, 0xc00, v1
	v_and_b32_e32 v26, 31, v0
	v_lshlrev_b32_e32 v26, 2, v26
	s_lshl_b32 s26, s0, 2
	v_add3_u32 v25, v25, v26, s26
	global_load_dword v4, v25, s[10:11] nt
	v_add_u32_e32 v26, 0x6000, v25
	global_load_dword v2, v26, s[10:11] nt
	v_add_u32_e32 v26, 0xc000, v25
	global_load_dword v10, v26, s[10:11] nt
	v_add_u32_e32 v26, 0x12000, v25
	global_load_dword v8, v26, s[10:11] nt
	v_add_u32_e32 v26, 0x18000, v25
	global_load_dword v5, v26, s[10:11] nt
	v_add_u32_e32 v26, 0x1e000, v25
	global_load_dword v3, v26, s[10:11] nt
	v_add_u32_e32 v26, 0x24000, v25
	global_load_dword v11, v26, s[10:11] nt
	v_add_u32_e32 v26, 0x2a000, v25
	global_load_dword v9, v26, s[10:11] nt
	v_add_u32_e32 v26, 0x30000, v25
	global_load_dword v14, v26, s[10:11] nt
	v_add_u32_e32 v26, 0x36000, v25
	global_load_dword v12, v26, s[10:11] nt
	v_add_u32_e32 v26, 0x3c000, v25
	global_load_dword v15, v26, s[10:11] nt
	v_add_u32_e32 v26, 0x42000, v25
	global_load_dword v13, v26, s[10:11] nt
	v_add_u32_e32 v26, 0x48000, v25
	global_load_dword v20, v26, s[10:11] nt
	v_add_u32_e32 v26, 0x4e000, v25
	global_load_dword v18, v26, s[10:11] nt
	v_add_u32_e32 v26, 0x54000, v25
	global_load_dword v23, v26, s[10:11] nt
	v_add_u32_e32 v26, 0x5a000, v25
	global_load_dword v22, v26, s[10:11] nt
	v_add_u32_e32 v26, 0x60000, v25
	global_load_dword v17, v26, s[10:11] nt
	v_add_u32_e32 v26, 0x66000, v25
	global_load_dword v24, v26, s[10:11] nt
	v_add_u32_e32 v26, 0x6c000, v25
	global_load_dword v21, v26, s[10:11] nt
	v_add_u32_e32 v27, 0x98, v1
	v_mov_b32_e32 v19, 0
	v_cmp_gt_i32_e32 vcc, s6, v27
	s_and_saveexec_b64 s[2:3], vcc
	s_cbranch_execz .LBB0_112
	v_add_u32_e32 v26, 0x72000, v25
	global_load_dword v19, v26, s[10:11] nt
